# phase-4 state-update loops: sign flips folded into the bf16 pack as source modifiers
# speedup vs baseline: 1.0059x; 1.0046x over previous
.LBB0_800:
	v_lshlrev_b32_e32 v36, 16, v158
	v_and_b32_e32 v37, 0xffff0000, v158
	v_lshlrev_b32_e32 v38, 16, v159
	v_and_b32_e32 v39, 0xffff0000, v159
	v_lshlrev_b32_e32 v40, 16, v154
	v_and_b32_e32 v41, 0xffff0000, v154
	v_lshlrev_b32_e32 v42, 16, v155
	v_and_b32_e32 v43, 0xffff0000, v155
	v_lshlrev_b32_e32 v44, 16, v152
	v_and_b32_e32 v45, 0xffff0000, v152
	v_lshlrev_b32_e32 v46, 16, v153
	v_and_b32_e32 v47, 0xffff0000, v153
	v_lshlrev_b32_e32 v48, 16, v150
	v_and_b32_e32 v49, 0xffff0000, v150
	v_lshlrev_b32_e32 v50, 16, v151
	v_and_b32_e32 v51, 0xffff0000, v151
	v_cvt_pk_bf16_f32 v116, -v20, -v21
	v_cvt_pk_bf16_f32 v117, -v22, -v23
	v_cvt_pk_bf16_f32 v118, -v24, -v25
	v_cvt_pk_bf16_f32 v119, -v26, -v27
	v_lshlrev_b32_e32 v52, 16, v164
	v_and_b32_e32 v53, 0xffff0000, v164
	v_mfma_f32_32x32x16_bf16 v[36:51], v[92:95], v[116:119], v[36:51]
	v_lshlrev_b32_e32 v54, 16, v165
	v_and_b32_e32 v55, 0xffff0000, v165
	v_lshlrev_b32_e32 v56, 16, v162
	v_and_b32_e32 v57, 0xffff0000, v162
	v_lshlrev_b32_e32 v58, 16, v163
	v_and_b32_e32 v59, 0xffff0000, v163
	v_lshlrev_b32_e32 v60, 16, v160
	v_and_b32_e32 v61, 0xffff0000, v160
	v_lshlrev_b32_e32 v62, 16, v161
	v_and_b32_e32 v63, 0xffff0000, v161
	v_lshlrev_b32_e32 v64, 16, v156
	v_and_b32_e32 v65, 0xffff0000, v156
	v_lshlrev_b32_e32 v66, 16, v157
	v_and_b32_e32 v67, 0xffff0000, v157
	s_add_i32 s18, s14, s15
	s_ashr_i32 s19, s18, 31
	v_mfma_f32_32x32x16_bf16 v[52:67], v[96:99], v[116:119], v[52:67]
	s_lshl_b64 s[4:5], s[18:19], 2
	v_cvt_pk_bf16_f32 v120, -v4, -v5
	v_cvt_pk_bf16_f32 v121, -v6, -v7
	v_cvt_pk_bf16_f32 v122, -v8, -v9
	v_cvt_pk_bf16_f32 v123, -v10, -v11
	s_add_u32 s8, s12, s4
	s_addc_u32 s9, s13, s5
	s_lshl_b64 s[6:7], s[18:19], 13
	v_mfma_f32_32x32x16_bf16 v[36:51], v[84:87], v[120:123], v[36:51]
	v_lshl_add_u64 v[96:97], v[136:137], 0, s[6:7]
	v_cvt_pk_bf16_f32 v124, -v28, -v29
	v_cvt_pk_bf16_f32 v125, -v30, -v31
	v_lshl_add_u64 v[150:151], v[96:97], 0, v[2:3]
	v_mfma_f32_32x32x16_bf16 v[52:67], v[88:91], v[120:123], v[52:67]
	v_cvt_pk_bf16_f32 v126, -v32, -v33
	global_load_dword v204, v3, s[8:9]
	v_lshl_add_u64 v[152:153], v[96:97], 0, v[142:143]
	global_load_dwordx4 v[96:99], v[150:151], off
	global_load_dwordx4 v[116:119], v[150:151], off offset:32
	s_add_i32 s4, s18, 4
	s_ashr_i32 s5, s4, 31
	s_lshl_b64 s[4:5], s[4:5], 13
	v_cvt_pk_bf16_f32 v127, -v34, -v35
	global_load_dwordx4 v[84:87], v[152:153], off
	global_load_dwordx4 v[128:131], v[152:153], off offset:32
	global_load_dwordx4 v[168:171], v[150:151], off offset:64
	global_load_dwordx4 v[172:175], v[150:151], off offset:96
	global_load_dwordx4 v[176:179], v[152:153], off offset:64
	global_load_dwordx4 v[180:183], v[152:153], off offset:96
	v_lshl_add_u64 v[150:151], v[134:135], 0, s[4:5]
	v_lshl_add_u64 v[88:89], v[146:147], 0, s[4:5]
	v_cvt_pk_bf16_f32 v92, -v12, -v13
	v_cvt_pk_bf16_f32 v93, -v14, -v15
	v_cvt_pk_bf16_f32 v94, -v16, -v17
	v_cvt_pk_bf16_f32 v95, -v18, -v19
	v_lshl_add_u64 v[120:121], v[150:151], 0, v[2:3]
	v_lshl_add_u64 v[196:197], v[150:151], 0, v[142:143]
	global_load_dwordx2 v[158:159], v[88:89], off
	global_load_dwordx2 v[154:155], v[88:89], off offset:16
	global_load_dwordx2 v[152:153], v[88:89], off offset:32
	v_mfma_f32_32x32x16_bf16 v[36:51], v[76:79], v[124:127], v[36:51]
	global_load_dwordx2 v[150:151], v[88:89], off offset:48
	global_load_dwordx2 v[164:165], v[88:89], off offset:64
	global_load_dwordx2 v[162:163], v[88:89], off offset:80
	global_load_dwordx2 v[160:161], v[88:89], off offset:96
	global_load_dwordx2 v[156:157], v[88:89], off offset:112
	global_load_dwordx4 v[76:79], v[120:121], off
	s_nop 0
	global_load_dwordx4 v[88:91], v[120:121], off offset:32
	v_cvt_pk_bf16_f32 v100, v20, v21
	v_cvt_pk_bf16_f32 v101, v22, v23
	v_cvt_pk_bf16_f32 v102, v4, v5
	v_cvt_pk_bf16_f32 v103, v6, v7
	v_cvt_pk_bf16_f32 v104, v24, v25
	v_cvt_pk_bf16_f32 v105, v26, v27
	v_mfma_f32_32x32x16_bf16 v[52:67], v[80:83], v[124:127], v[52:67]
	global_load_dwordx4 v[80:83], v[120:121], off offset:64
	s_nop 0
	global_load_dwordx4 v[120:123], v[120:121], off offset:96
	s_nop 0
	global_load_dwordx4 v[184:187], v[196:197], off
	global_load_dwordx4 v[188:191], v[196:197], off offset:32
	global_load_dwordx4 v[192:195], v[196:197], off offset:64
	s_nop 0
	global_load_dwordx4 v[196:199], v[196:197], off offset:96
	v_lshl_add_u64 v[206:207], v[148:149], 0, s[6:7]
	v_cvt_pk_bf16_f32 v106, v8, v9
	v_cvt_pk_bf16_f32 v107, v10, v11
	v_cvt_pk_bf16_f32 v108, v28, v29
	v_cvt_pk_bf16_f32 v109, v30, v31
	v_cvt_pk_bf16_f32 v110, v12, v13
	v_mfma_f32_32x32x16_bf16 v[36:51], v[68:71], v[92:95], v[36:51]
	v_cvt_pk_bf16_f32 v111, v14, v15
	v_cvt_pk_bf16_f32 v112, v32, v33
	v_cvt_pk_bf16_f32 v113, v34, v35
	v_cvt_pk_bf16_f32 v114, v16, v17
	v_cvt_pk_bf16_f32 v115, v18, v19
	global_store_dwordx2 v[206:207], v[100:101], off
	global_store_dwordx2 v[206:207], v[102:103], off offset:64
	global_store_dwordx2 v[206:207], v[104:105], off offset:16
	global_store_dwordx2 v[206:207], v[106:107], off offset:80
	global_store_dwordx2 v[206:207], v[108:109], off offset:32
	global_store_dwordx2 v[206:207], v[110:111], off offset:96
	global_store_dwordx2 v[206:207], v[112:113], off offset:48
	global_store_dwordx2 v[206:207], v[114:115], off offset:112
	v_mfma_f32_32x32x16_bf16 v[52:67], v[72:75], v[92:95], v[52:67]
	v_cvt_pk_bf16_f32 v36, v36, v37
	v_cvt_pk_bf16_f32 v37, v38, v39
	v_cvt_pk_bf16_f32 v39, v42, v43
	v_cvt_pk_bf16_f32 v42, v48, v49
	v_cvt_pk_bf16_f32 v38, v40, v41
	v_cvt_pk_bf16_f32 v40, v44, v45
	v_cvt_pk_bf16_f32 v43, v50, v51
	s_nop 4
	v_cvt_pk_bf16_f32 v52, v52, v53
	v_cvt_pk_bf16_f32 v53, v54, v55
	v_cvt_pk_bf16_f32 v54, v56, v57
	v_cvt_pk_bf16_f32 v44, v60, v61
	v_cvt_pk_bf16_f32 v45, v62, v63
	v_cvt_pk_bf16_f32 v41, v46, v47
	v_cvt_pk_bf16_f32 v46, v64, v65
	v_lshl_add_u64 v[208:209], v[146:147], 0, s[6:7]
	v_cvt_pk_bf16_f32 v55, v58, v59
	v_cvt_pk_bf16_f32 v47, v66, v67
	global_store_dwordx2 v[208:209], v[36:37], off
	global_store_dwordx2 v[208:209], v[52:53], off offset:64
	global_store_dwordx2 v[208:209], v[38:39], off offset:16
	global_store_dwordx2 v[208:209], v[54:55], off offset:80
	global_store_dwordx2 v[208:209], v[40:41], off offset:32
	global_store_dwordx2 v[208:209], v[44:45], off offset:96
	global_store_dwordx2 v[208:209], v[42:43], off offset:48
	global_store_dwordx2 v[208:209], v[46:47], off offset:112
	s_add_i32 s15, s15, 4
	s_cmpk_lg_i32 s15, 0xfc
	s_waitcnt vmcnt(40)
	v_pk_mul_f32 v[34:35], v[34:35], v[204:205] op_sel_hi:[1,0]
	s_waitcnt vmcnt(39)
	v_cndmask_b32_e32 v48, v96, v98, vcc
	v_cndmask_b32_e32 v49, v97, v99, vcc
	ds_bpermute_b32 v48, v166, v48
	ds_bpermute_b32 v49, v166, v49
	s_waitcnt vmcnt(38)
	v_cndmask_b32_e32 v50, v116, v118, vcc
	v_cndmask_b32_e32 v51, v117, v119, vcc
	ds_bpermute_b32 v68, v166, v50
	ds_bpermute_b32 v69, v166, v51
	v_pk_mul_f32 v[32:33], v[32:33], v[204:205] op_sel_hi:[1,0]
	v_pk_mul_f32 v[30:31], v[30:31], v[204:205] op_sel_hi:[1,0]
	v_pk_mul_f32 v[28:29], v[28:29], v[204:205] op_sel_hi:[1,0]
	s_waitcnt vmcnt(37)
	v_cndmask_b32_e32 v56, v84, v86, vcc
	v_cndmask_b32_e32 v57, v85, v87, vcc
	ds_bpermute_b32 v70, v166, v56
	ds_bpermute_b32 v71, v166, v57
	s_waitcnt vmcnt(35)
	v_cndmask_b32_e32 v60, v168, v170, vcc
	v_cndmask_b32_e32 v61, v169, v171, vcc
	s_waitcnt vmcnt(34)
	v_cndmask_b32_e32 v62, v172, v174, vcc
	v_cndmask_b32_e32 v63, v173, v175, vcc
	ds_bpermute_b32 v74, v166, v60
	ds_bpermute_b32 v75, v166, v61
	ds_bpermute_b32 v92, v166, v62
	ds_bpermute_b32 v93, v166, v63
	v_pk_mul_f32 v[26:27], v[26:27], v[204:205] op_sel_hi:[1,0]
	v_pk_mul_f32 v[24:25], v[24:25], v[204:205] op_sel_hi:[1,0]
	v_pk_mul_f32 v[22:23], v[22:23], v[204:205] op_sel_hi:[1,0]
	s_waitcnt vmcnt(23)
	v_cndmask_b32_e32 v50, v76, v78, vcc
	v_cndmask_b32_e32 v51, v77, v79, vcc
	v_pk_mul_f32 v[20:21], v[20:21], v[204:205] op_sel_hi:[1,0]
	v_pk_mul_f32 v[18:19], v[18:19], v[204:205] op_sel_hi:[1,0]
	v_pk_mul_f32 v[16:17], v[16:17], v[204:205] op_sel_hi:[1,0]
	s_waitcnt vmcnt(20)
	v_cndmask_b32_e32 v60, v120, v122, vcc
	v_cndmask_b32_e32 v61, v121, v123, vcc
	s_waitcnt vmcnt(19)
	v_cndmask_b32_e32 v62, v184, v186, vcc
	v_cndmask_b32_e32 v63, v185, v187, vcc
	v_pk_mul_f32 v[14:15], v[14:15], v[204:205] op_sel_hi:[1,0]
	v_pk_mul_f32 v[12:13], v[12:13], v[204:205] op_sel_hi:[1,0]
	v_pk_mul_f32 v[10:11], v[10:11], v[204:205] op_sel_hi:[1,0]
	v_pk_mul_f32 v[8:9], v[8:9], v[204:205] op_sel_hi:[1,0]
	v_pk_mul_f32 v[6:7], v[6:7], v[204:205] op_sel_hi:[1,0]
	v_pk_mul_f32 v[4:5], v[4:5], v[204:205] op_sel_hi:[1,0]
	ds_bpermute_b32 v104, v166, v50
	ds_bpermute_b32 v105, v166, v51
	ds_bpermute_b32 v145, v166, v60
	ds_bpermute_b32 v167, v166, v61
	ds_bpermute_b32 v203, v166, v62
	ds_bpermute_b32 v204, v166, v63
	s_waitcnt lgkmcnt(14)
	v_cndmask_b32_e32 v51, v99, v49, vcc
	v_cndmask_b32_e32 v50, v98, v48, vcc
	v_cndmask_b32_e32 v49, v49, v97, vcc
	v_cndmask_b32_e32 v48, v48, v96, vcc
	s_waitcnt lgkmcnt(10)
	v_cndmask_b32_e32 v63, v87, v71, vcc
	v_cndmask_b32_e32 v62, v86, v70, vcc
	v_cndmask_b32_e32 v61, v71, v85, vcc
	v_cndmask_b32_e32 v60, v70, v84, vcc
	v_cndmask_b32_e32 v64, v176, v178, vcc
	v_cndmask_b32_e32 v65, v177, v179, vcc
	ds_bpermute_b32 v94, v166, v64
	ds_bpermute_b32 v95, v166, v65
	v_mfma_f32_32x32x16_bf16 v[20:35], v[48:51], v[36:39], v[20:35]
	s_waitcnt lgkmcnt(10)
	v_cndmask_b32_e32 v51, v171, v75, vcc
	v_cndmask_b32_e32 v50, v170, v74, vcc
	v_cndmask_b32_e32 v49, v75, v169, vcc
	v_cndmask_b32_e32 v48, v74, v168, vcc
	v_cndmask_b32_e32 v58, v128, v130, vcc
	v_cndmask_b32_e32 v59, v129, v131, vcc
	ds_bpermute_b32 v72, v166, v58
	v_mfma_f32_32x32x16_bf16 v[4:19], v[60:63], v[36:39], v[4:19]
	s_waitcnt lgkmcnt(1)
	v_cndmask_b32_e32 v39, v179, v95, vcc
	v_cndmask_b32_e32 v38, v178, v94, vcc
	v_cndmask_b32_e32 v37, v95, v177, vcc
	v_cndmask_b32_e32 v36, v94, v176, vcc
	ds_bpermute_b32 v73, v166, v59
	v_cndmask_b32_e32 v66, v180, v182, vcc
	v_cndmask_b32_e32 v67, v181, v183, vcc
	v_mfma_f32_32x32x16_bf16 v[20:35], v[48:51], v[52:55], v[20:35]
	ds_bpermute_b32 v100, v166, v66
	ds_bpermute_b32 v101, v166, v67
	v_cndmask_b32_e32 v56, v88, v90, vcc
	v_cndmask_b32_e32 v57, v89, v91, vcc
	v_cndmask_b32_e32 v58, v80, v82, vcc
	v_cndmask_b32_e32 v59, v81, v83, vcc
	s_waitcnt vmcnt(18)
	v_cndmask_b32_e32 v64, v188, v190, vcc
	v_mfma_f32_32x32x16_bf16 v[4:19], v[36:39], v[52:55], v[4:19]
	v_cndmask_b32_e32 v65, v189, v191, vcc
	s_waitcnt vmcnt(17)
	v_cndmask_b32_e32 v66, v192, v194, vcc
	v_cndmask_b32_e32 v67, v193, v195, vcc
	ds_bpermute_b32 v106, v166, v56
	ds_bpermute_b32 v107, v166, v57
	ds_bpermute_b32 v108, v166, v58
	ds_bpermute_b32 v109, v166, v59
	ds_bpermute_b32 v205, v166, v64
	ds_bpermute_b32 v206, v166, v65
	ds_bpermute_b32 v207, v166, v66
	ds_bpermute_b32 v208, v166, v67
	v_cndmask_b32_e32 v59, v119, v69, vcc
	v_cndmask_b32_e32 v58, v118, v68, vcc
	v_cndmask_b32_e32 v57, v69, v117, vcc
	v_cndmask_b32_e32 v56, v68, v116, vcc
	s_waitcnt lgkmcnt(10)
	v_cndmask_b32_e32 v67, v131, v73, vcc
	v_cndmask_b32_e32 v66, v130, v72, vcc
	v_cndmask_b32_e32 v65, v73, v129, vcc
	v_cndmask_b32_e32 v64, v72, v128, vcc
	v_mfma_f32_32x32x16_bf16 v[20:35], v[56:59], v[40:43], v[20:35]
	v_cndmask_b32_e32 v71, v175, v93, vcc
	v_cndmask_b32_e32 v70, v174, v92, vcc
	v_cndmask_b32_e32 v69, v93, v173, vcc
	v_cndmask_b32_e32 v68, v92, v172, vcc
	s_waitcnt lgkmcnt(8)
	v_cndmask_b32_e32 v63, v183, v101, vcc
	v_cndmask_b32_e32 v62, v182, v100, vcc
	v_cndmask_b32_e32 v61, v101, v181, vcc
	v_mfma_f32_32x32x16_bf16 v[4:19], v[64:67], v[40:43], v[4:19]
	v_cndmask_b32_e32 v60, v100, v180, vcc
	s_waitcnt vmcnt(16)
	v_cndmask_b32_e32 v102, v196, v198, vcc
	v_cndmask_b32_e32 v103, v197, v199, vcc
	ds_bpermute_b32 v209, v166, v102
	ds_bpermute_b32 v210, v166, v103
	v_cndmask_b32_e32 v131, v79, v105, vcc
	v_cndmask_b32_e32 v130, v78, v104, vcc
	v_mfma_f32_32x32x16_bf16 v[20:35], v[68:71], v[44:47], v[20:35]
	v_cndmask_b32_e32 v129, v105, v77, vcc
	v_cndmask_b32_e32 v128, v104, v76, vcc
	s_waitcnt lgkmcnt(8)
	v_cndmask_b32_e32 v113, v107, v89, vcc
	v_cndmask_b32_e32 v112, v106, v88, vcc
	s_waitcnt lgkmcnt(6)
	v_cndmask_b32_e32 v127, v83, v109, vcc
	v_cndmask_b32_e32 v126, v82, v108, vcc
	v_cndmask_b32_e32 v125, v109, v81, vcc
	v_mfma_f32_32x32x16_bf16 v[4:19], v[60:63], v[44:47], v[4:19]
	v_cndmask_b32_e32 v124, v108, v80, vcc
	v_cndmask_b32_e32 v109, v167, v121, vcc
	v_cndmask_b32_e32 v108, v145, v120, vcc
	v_cndmask_b32_e32 v121, v204, v185, vcc
	v_cndmask_b32_e32 v120, v203, v184, vcc
	s_waitcnt lgkmcnt(4)
	v_cndmask_b32_e32 v105, v206, v189, vcc
	v_cndmask_b32_e32 v104, v205, v188, vcc
	s_waitcnt lgkmcnt(2)
	v_cndmask_b32_e32 v117, v208, v193, vcc
	v_cndmask_b32_e32 v116, v207, v192, vcc
	s_waitcnt lgkmcnt(0)
	v_cndmask_b32_e32 v101, v210, v197, vcc
	v_cndmask_b32_e32 v100, v209, v196, vcc
	v_cndmask_b32_e32 v115, v91, v107, vcc
	v_cndmask_b32_e32 v114, v90, v106, vcc
	v_cndmask_b32_e32 v111, v123, v167, vcc
	v_cndmask_b32_e32 v110, v122, v145, vcc
	v_cndmask_b32_e32 v123, v187, v204, vcc
	v_cndmask_b32_e32 v122, v186, v203, vcc
	v_cndmask_b32_e32 v107, v191, v206, vcc
	v_cndmask_b32_e32 v106, v190, v205, vcc
	v_cndmask_b32_e32 v119, v195, v208, vcc
	v_cndmask_b32_e32 v118, v194, v207, vcc
	v_cndmask_b32_e32 v103, v199, v210, vcc
	v_cndmask_b32_e32 v102, v198, v209, vcc
	v_mov_b64_e32 v[72:73], v[100:101]
	v_mov_b64_e32 v[88:89], v[116:117]
	v_mov_b64_e32 v[80:81], v[104:105]
	v_mov_b64_e32 v[96:97], v[120:121]
	v_mov_b64_e32 v[68:69], v[108:109]
	v_mov_b64_e32 v[84:85], v[124:125]
	v_mov_b64_e32 v[76:77], v[112:113]
	v_mov_b64_e32 v[92:93], v[128:129]
	v_mov_b64_e32 v[74:75], v[102:103]
	v_mov_b64_e32 v[90:91], v[118:119]
	v_mov_b64_e32 v[82:83], v[106:107]
	v_mov_b64_e32 v[98:99], v[122:123]
	v_mov_b64_e32 v[70:71], v[110:111]
	v_mov_b64_e32 v[86:87], v[126:127]
	v_mov_b64_e32 v[78:79], v[114:115]
	v_mov_b64_e32 v[94:95], v[130:131]
	s_cbranch_scc1 .LBB0_800
	v_cvt_pk_bf16_f32 v70, v20, v21
	v_cvt_pk_bf16_f32 v20, -v20, -v21
	v_cvt_pk_bf16_f32 v71, v22, v23
	v_cvt_pk_bf16_f32 v21, -v22, -v23
	v_cvt_pk_bf16_f32 v22, -v24, -v25
	v_lshlrev_b32_e32 v52, 16, v158
	v_and_b32_e32 v53, 0xffff0000, v158
	v_lshlrev_b32_e32 v54, 16, v159
	v_and_b32_e32 v55, 0xffff0000, v159
	v_lshlrev_b32_e32 v56, 16, v154
	v_and_b32_e32 v57, 0xffff0000, v154
	v_lshlrev_b32_e32 v58, 16, v155
	v_and_b32_e32 v59, 0xffff0000, v155
	v_lshlrev_b32_e32 v60, 16, v152
	v_and_b32_e32 v61, 0xffff0000, v152
	v_lshlrev_b32_e32 v62, 16, v153
	v_and_b32_e32 v63, 0xffff0000, v153
	v_lshlrev_b32_e32 v64, 16, v150
	v_and_b32_e32 v65, 0xffff0000, v150
	v_lshlrev_b32_e32 v66, 16, v151
	v_and_b32_e32 v67, 0xffff0000, v151
	v_cvt_pk_bf16_f32 v23, -v26, -v27
	v_lshlrev_b32_e32 v36, 16, v164
	v_and_b32_e32 v37, 0xffff0000, v164
	v_lshlrev_b32_e32 v38, 16, v165
	v_and_b32_e32 v39, 0xffff0000, v165
	v_lshlrev_b32_e32 v40, 16, v162
	v_and_b32_e32 v41, 0xffff0000, v162
	v_lshlrev_b32_e32 v42, 16, v163
	v_and_b32_e32 v43, 0xffff0000, v163
	v_lshlrev_b32_e32 v44, 16, v160
	v_and_b32_e32 v45, 0xffff0000, v160
	v_lshlrev_b32_e32 v46, 16, v161
	v_and_b32_e32 v47, 0xffff0000, v161
	v_lshlrev_b32_e32 v48, 16, v156
	v_and_b32_e32 v49, 0xffff0000, v156
	v_lshlrev_b32_e32 v50, 16, v157
	v_and_b32_e32 v51, 0xffff0000, v157
	v_mfma_f32_32x32x16_bf16 v[52:67], v[128:131], v[20:23], v[52:67]
	v_cvt_pk_bf16_f32 v72, v4, v5
	v_cvt_pk_bf16_f32 v4, -v4, -v5
	v_cvt_pk_bf16_f32 v73, v6, v7
	v_mfma_f32_32x32x16_bf16 v[36:51], v[120:123], v[20:23], v[36:51]
	v_cvt_pk_bf16_f32 v5, -v6, -v7
	v_cvt_pk_bf16_f32 v6, -v8, -v9
	v_cvt_pk_bf16_f32 v7, -v10, -v11
	s_or_b32 s4, s20, s17
	v_mfma_f32_32x32x16_bf16 v[52:67], v[124:127], v[4:7], v[52:67]
	s_or_b32 s4, s4, 0xfc
	s_ashr_i32 s5, s4, 31
	s_lshl_b64 s[14:15], s[4:5], 13
	v_lshl_add_u64 v[68:69], v[148:149], 0, s[14:15]
	global_store_dwordx2 v[68:69], v[70:71], off
	global_store_dwordx2 v[68:69], v[72:73], off offset:64
	v_cvt_pk_bf16_f32 v72, v8, v9
	v_mfma_f32_32x32x16_bf16 v[36:51], v[116:119], v[4:7], v[36:51]
	v_cvt_pk_bf16_f32 v4, -v28, -v29
	v_cvt_pk_bf16_f32 v5, -v30, -v31
	v_cvt_pk_bf16_f32 v6, -v32, -v33
	v_cvt_pk_bf16_f32 v7, -v34, -v35
	v_cvt_pk_bf16_f32 v8, -v12, -v13
	v_mfma_f32_32x32x16_bf16 v[52:67], v[112:115], v[4:7], v[52:67]
	v_cvt_pk_bf16_f32 v73, v10, v11
	v_cvt_pk_bf16_f32 v9, -v14, -v15
	v_cvt_pk_bf16_f32 v10, -v16, -v17
	v_mfma_f32_32x32x16_bf16 v[36:51], v[104:107], v[4:7], v[36:51]
	v_xor_b32_e32 v2, 0x80000000, v18
	v_xor_b32_e32 v11, 0x80000000, v19
	v_cvt_pk_bf16_f32 v11, v2, v11
	v_cvt_pk_bf16_f32 v70, v24, v25
	v_cvt_pk_bf16_f32 v71, v26, v27
	global_store_dwordx2 v[68:69], v[70:71], off offset:16
	global_store_dwordx2 v[68:69], v[72:73], off offset:80
	v_cvt_pk_bf16_f32 v70, v28, v29
	v_mfma_f32_32x32x16_bf16 v[52:67], v[108:111], v[8:11], v[52:67]
	v_cvt_pk_bf16_f32 v71, v30, v31
	v_cvt_pk_bf16_f32 v72, v12, v13
	v_cvt_pk_bf16_f32 v73, v14, v15
	global_store_dwordx2 v[68:69], v[70:71], off offset:32
	global_store_dwordx2 v[68:69], v[72:73], off offset:96
	v_cvt_pk_bf16_f32 v70, v32, v33
	v_cvt_pk_bf16_f32 v71, v34, v35
	v_lshl_add_u64 v[4:5], v[146:147], 0, s[14:15]
	v_mfma_f32_32x32x16_bf16 v[36:51], v[100:103], v[8:11], v[36:51]
	s_nop 2
	v_cvt_pk_bf16_f32 v6, v52, v53
	v_cvt_pk_bf16_f32 v7, v54, v55
	v_cvt_pk_bf16_f32 v72, v16, v17
	v_cvt_pk_bf16_f32 v73, v18, v19
	global_store_dwordx2 v[68:69], v[70:71], off offset:48
	global_store_dwordx2 v[68:69], v[72:73], off offset:112
	s_add_i32 s16, s16, s54
	s_cmp_lt_i32 s16, 64
	s_nop 0
	v_cvt_pk_bf16_f32 v8, v36, v37
	v_cvt_pk_bf16_f32 v9, v38, v39
	global_store_dwordx2 v[4:5], v[6:7], off
	global_store_dwordx2 v[4:5], v[8:9], off offset:64
	v_cvt_pk_bf16_f32 v6, v56, v57
	v_cvt_pk_bf16_f32 v7, v58, v59
	v_cvt_pk_bf16_f32 v8, v40, v41
	v_cvt_pk_bf16_f32 v9, v42, v43
	global_store_dwordx2 v[4:5], v[6:7], off offset:16
	global_store_dwordx2 v[4:5], v[8:9], off offset:80
	v_cvt_pk_bf16_f32 v6, v60, v61
	v_cvt_pk_bf16_f32 v7, v62, v63
	v_cvt_pk_bf16_f32 v8, v44, v45
	v_cvt_pk_bf16_f32 v9, v46, v47
	global_store_dwordx2 v[4:5], v[6:7], off offset:32
	global_store_dwordx2 v[4:5], v[8:9], off offset:96
	v_cvt_pk_bf16_f32 v6, v64, v65
	v_cvt_pk_bf16_f32 v7, v66, v67
	v_cvt_pk_bf16_f32 v8, v48, v49
	v_cvt_pk_bf16_f32 v9, v50, v51
	global_store_dwordx2 v[4:5], v[6:7], off offset:48
	global_store_dwordx2 v[4:5], v[8:9], off offset:112
	s_cbranch_scc1 .LBB0_799
